# speedup vs baseline: 1.0235x; 1.0235x over previous
.Lk1_nowarm9:
	s_mov_b32 s40, 0
	s_add_u32 s41, s40, s13
	s_add_u32 s42, s41, s13
	s_add_u32 s43, s42, s13
	s_add_u32 s44, s43, s13
	s_add_u32 s45, s44, s13
	s_add_u32 s46, s45, s13
	s_add_u32 s47, s46, s13
	s_add_u32 s48, s47, s13
	s_add_u32 s49, s48, s13
	s_add_u32 s50, s49, s13
	s_add_u32 s51, s50, s13
	s_add_u32 s52, s51, s13
	s_add_u32 s53, s52, s13
	s_add_u32 s54, s53, s13
	s_add_u32 s55, s54, s13
	buffer_load_dword v8, v1, s[8:11], s40 offen nt
	buffer_load_dword v9, v1, s[8:11], s41 offen nt
	buffer_load_dword v10, v1, s[8:11], s42 offen nt
	buffer_load_dword v11, v1, s[8:11], s43 offen nt
	buffer_load_dword v12, v1, s[8:11], s44 offen nt
	buffer_load_dword v13, v1, s[8:11], s45 offen nt
	buffer_load_dword v14, v1, s[8:11], s46 offen nt
	buffer_load_dword v15, v1, s[8:11], s47 offen nt
	buffer_load_dword v16, v1, s[8:11], s48 offen nt
	buffer_load_dword v17, v1, s[8:11], s49 offen nt
	buffer_load_dword v18, v1, s[8:11], s50 offen nt
	buffer_load_dword v19, v1, s[8:11], s51 offen nt
	buffer_load_dword v20, v1, s[8:11], s52 offen nt
	buffer_load_dword v21, v1, s[8:11], s53 offen nt
	buffer_load_dword v22, v1, s[8:11], s54 offen nt
	buffer_load_dword v23, v1, s[8:11], s55 offen nt
	s_add_u32 s8, s8, 0x4e200
	s_addc_u32 s9, s9, 0
	buffer_load_dword v24, v1, s[8:11], s40 offen nt
	buffer_load_dword v25, v1, s[8:11], s41 offen nt
	buffer_load_dword v26, v1, s[8:11], s42 offen nt
	buffer_load_dword v27, v1, s[8:11], s43 offen nt
	buffer_load_dword v28, v1, s[8:11], s44 offen nt
	buffer_load_dword v29, v1, s[8:11], s45 offen nt
	buffer_load_dword v30, v1, s[8:11], s46 offen nt
	buffer_load_dword v31, v1, s[8:11], s47 offen nt
	buffer_load_dword v32, v1, s[8:11], s48 offen nt
	buffer_load_dword v33, v1, s[8:11], s49 offen nt
	buffer_load_dword v34, v1, s[8:11], s50 offen nt
	buffer_load_dword v35, v1, s[8:11], s51 offen nt
	buffer_load_dword v36, v1, s[8:11], s52 offen nt
	buffer_load_dword v37, v1, s[8:11], s53 offen nt
	buffer_load_dword v38, v1, s[8:11], s54 offen nt
	buffer_load_dword v39, v1, s[8:11], s55 offen nt
	s_add_u32 s8, s8, 0x4e200
	s_addc_u32 s9, s9, 0
	buffer_load_dword v40, v1, s[8:11], s40 offen nt
	buffer_load_dword v41, v1, s[8:11], s41 offen nt
	buffer_load_dword v42, v1, s[8:11], s42 offen nt
	buffer_load_dword v43, v1, s[8:11], s43 offen nt
	buffer_load_dword v44, v1, s[8:11], s44 offen nt
	buffer_load_dword v45, v1, s[8:11], s45 offen nt
	buffer_load_dword v46, v1, s[8:11], s46 offen nt
	buffer_load_dword v47, v1, s[8:11], s47 offen nt
	buffer_load_dword v48, v1, s[8:11], s48 offen nt
	buffer_load_dword v49, v1, s[8:11], s49 offen nt
	buffer_load_dword v50, v1, s[8:11], s50 offen nt
	buffer_load_dword v51, v1, s[8:11], s51 offen nt
	buffer_load_dword v52, v1, s[8:11], s52 offen nt
	buffer_load_dword v53, v1, s[8:11], s53 offen nt
	buffer_load_dword v54, v1, s[8:11], s54 offen nt
	buffer_load_dword v55, v1, s[8:11], s55 offen nt
	v_mul_u32_u24_e32 v3, 0x147b, v2
	v_lshrrev_b32_e32 v3, 19, v3
	v_mul_u32_u24_e32 v98, 0x64, v3
	v_sub_u32_e32 v98, v2, v98
	v_add_u32_e32 v3, -1, v3
	v_add_u32_e32 v98, -1, v98
	s_movk_i32 s17, 0x62
	v_cmp_gt_u32_e64 s[36:37], 48, v3
	v_cmp_gt_u32_e64 s[38:39], s17, v98
	s_mul_i32 s17, s15, 0x1388
	v_add_lshl_u32 v98, v2, s17, 3
	s_and_b64 s[36:37], s[36:37], s[38:39]
	s_waitcnt vmcnt(32)
	v_max3_f32 v76, v8, v9, v10
	v_max3_f32 v76, v76, v11, v12
	v_max3_f32 v76, v76, v13, v14
	v_max3_f32 v76, v76, v15, v16
	v_max3_f32 v76, v76, v17, v18
	v_max3_f32 v76, v76, v19, v20
	v_max3_f32 v76, v76, v21, v22
	v_max_f32_e32 v76, v76, v23
	v_sub_f32_e32 v8, v8, v76
	v_sub_f32_e32 v9, v9, v76
	v_sub_f32_e32 v10, v10, v76
	v_sub_f32_e32 v11, v11, v76
	v_sub_f32_e32 v12, v12, v76
	v_sub_f32_e32 v13, v13, v76
	v_sub_f32_e32 v14, v14, v76
	v_sub_f32_e32 v15, v15, v76
	v_sub_f32_e32 v16, v16, v76
	v_sub_f32_e32 v17, v17, v76
	v_sub_f32_e32 v18, v18, v76
	v_sub_f32_e32 v19, v19, v76
	v_sub_f32_e32 v20, v20, v76
	v_sub_f32_e32 v21, v21, v76
	v_sub_f32_e32 v22, v22, v76
	v_sub_f32_e32 v23, v23, v76
	v_or_b32_e32 v81, 0, v8
	v_or_b32_e32 v82, 1, v9
	v_min_u32_e32 v80, v81, v82
	v_or_b32_e32 v81, 2, v10
	v_or_b32_e32 v82, 3, v11
	v_min3_u32 v80, v80, v81, v82
	v_or_b32_e32 v81, 4, v12
	v_or_b32_e32 v82, 5, v13
	v_min3_u32 v80, v80, v81, v82
	v_or_b32_e32 v81, 6, v14
	v_or_b32_e32 v82, 7, v15
	v_min3_u32 v80, v80, v81, v82
	v_or_b32_e32 v81, 8, v16
	v_or_b32_e32 v82, 9, v17
	v_min3_u32 v80, v80, v81, v82
	v_or_b32_e32 v81, 10, v18
	v_or_b32_e32 v82, 11, v19
	v_min3_u32 v80, v80, v81, v82
	v_or_b32_e32 v81, 12, v20
	v_or_b32_e32 v82, 13, v21
	v_min3_u32 v80, v80, v81, v82
	v_or_b32_e32 v81, 14, v22
	v_or_b32_e32 v82, 15, v23
	v_min3_u32 v80, v80, v81, v82
	v_mul_f32_e32 v8, s14, v8
	v_mul_f32_e32 v9, s14, v9
	v_mul_f32_e32 v10, s14, v10
	v_mul_f32_e32 v11, s14, v11
	v_mul_f32_e32 v12, s14, v12
	v_mul_f32_e32 v13, s14, v13
	v_mul_f32_e32 v14, s14, v14
	v_mul_f32_e32 v15, s14, v15
	v_mul_f32_e32 v16, s14, v16
	v_mul_f32_e32 v17, s14, v17
	v_mul_f32_e32 v18, s14, v18
	v_mul_f32_e32 v19, s14, v19
	v_mul_f32_e32 v20, s14, v20
	v_mul_f32_e32 v21, s14, v21
	v_mul_f32_e32 v22, s14, v22
	v_mul_f32_e32 v23, s14, v23
	v_exp_f32_e32 v8, v8
	v_exp_f32_e32 v9, v9
	v_exp_f32_e32 v10, v10
	v_exp_f32_e32 v11, v11
	v_exp_f32_e32 v12, v12
	v_exp_f32_e32 v13, v13
	v_exp_f32_e32 v14, v14
	v_exp_f32_e32 v15, v15
	v_exp_f32_e32 v16, v16
	v_exp_f32_e32 v17, v17
	v_exp_f32_e32 v18, v18
	v_exp_f32_e32 v19, v19
	v_exp_f32_e32 v20, v20
	v_exp_f32_e32 v21, v21
	v_exp_f32_e32 v22, v22
	v_exp_f32_e32 v23, v23
	v_add_f32_e32 v78, v8, v10
	v_add_f32_e32 v79, v9, v11
	v_add_f32_e32 v78, v78, v12
	v_add_f32_e32 v79, v79, v13
	v_add_f32_e32 v78, v78, v14
	v_add_f32_e32 v79, v79, v15
	v_add_f32_e32 v78, v78, v16
	v_add_f32_e32 v79, v79, v17
	v_add_f32_e32 v78, v78, v18
	v_add_f32_e32 v79, v79, v19
	v_add_f32_e32 v78, v78, v20
	v_add_f32_e32 v79, v79, v21
	v_add_f32_e32 v78, v78, v22
	v_add_f32_e32 v79, v79, v23
	v_add_f32_e32 v78, v78, v79
	v_cvt_f64_f32_e32 v[86:87], v78
	v_mov_b32_e32 v75, v80
	v_mov_b32_e32 v73, v76
	s_add_u32 s8, s8, 0x4e200
	s_addc_u32 s9, s9, 0
	buffer_load_dword v56, v1, s[8:11], s40 offen nt
	buffer_load_dword v57, v1, s[8:11], s41 offen nt
	buffer_load_dword v58, v1, s[8:11], s42 offen nt
	buffer_load_dword v59, v1, s[8:11], s43 offen nt
	buffer_load_dword v60, v1, s[8:11], s44 offen nt
	buffer_load_dword v61, v1, s[8:11], s45 offen nt
	buffer_load_dword v62, v1, s[8:11], s46 offen nt
	buffer_load_dword v63, v1, s[8:11], s47 offen nt
	buffer_load_dword v64, v1, s[8:11], s48 offen nt
	buffer_load_dword v65, v1, s[8:11], s49 offen nt
	buffer_load_dword v66, v1, s[8:11], s50 offen nt
	buffer_load_dword v67, v1, s[8:11], s51 offen nt
	buffer_load_dword v68, v1, s[8:11], s52 offen nt
	buffer_load_dword v69, v1, s[8:11], s53 offen nt
	buffer_load_dword v70, v1, s[8:11], s54 offen nt
	buffer_load_dword v71, v1, s[8:11], s55 offen nt
	s_add_u32 s8, s8, 0x4e200
	s_addc_u32 s9, s9, 0
	buffer_load_dword v72, v1, s[8:11], s40 offen nt
	s_waitcnt vmcnt(33)
	v_max3_f32 v76, v24, v25, v26
	v_max3_f32 v76, v76, v27, v28
	v_max3_f32 v76, v76, v29, v30
	v_max3_f32 v76, v76, v31, v32
	v_max3_f32 v76, v76, v33, v34
	v_max3_f32 v76, v76, v35, v36
	v_max3_f32 v76, v76, v37, v38
	v_max_f32_e32 v76, v76, v39
	v_max_f32_e32 v77, v73, v76
	v_cmp_gt_f32_e64 s[20:21], v76, v73
	v_sub_f32_e32 v83, v73, v77
	v_mul_f32_e32 v83, s14, v83
	v_exp_f32_e32 v83, v83
	v_sub_f32_e32 v24, v24, v77
	v_sub_f32_e32 v25, v25, v77
	v_sub_f32_e32 v26, v26, v77
	v_sub_f32_e32 v27, v27, v77
	v_sub_f32_e32 v28, v28, v77
	v_sub_f32_e32 v29, v29, v77
	v_sub_f32_e32 v30, v30, v77
	v_sub_f32_e32 v31, v31, v77
	v_sub_f32_e32 v32, v32, v77
	v_sub_f32_e32 v33, v33, v77
	v_sub_f32_e32 v34, v34, v77
	v_sub_f32_e32 v35, v35, v77
	v_sub_f32_e32 v36, v36, v77
	v_sub_f32_e32 v37, v37, v77
	v_sub_f32_e32 v38, v38, v77
	v_sub_f32_e32 v39, v39, v77
	v_cvt_f64_f32_e32 v[84:85], v83
	v_or_b32_e32 v81, 16, v24
	v_or_b32_e32 v82, 17, v25
	v_min_u32_e32 v80, v81, v82
	v_or_b32_e32 v81, 18, v26
	v_or_b32_e32 v82, 19, v27
	v_min3_u32 v80, v80, v81, v82
	v_or_b32_e32 v81, 20, v28
	v_or_b32_e32 v82, 21, v29
	v_min3_u32 v80, v80, v81, v82
	v_or_b32_e32 v81, 22, v30
	v_or_b32_e32 v82, 23, v31
	v_min3_u32 v80, v80, v81, v82
	v_or_b32_e32 v81, 24, v32
	v_or_b32_e32 v82, 25, v33
	v_min3_u32 v80, v80, v81, v82
	v_or_b32_e32 v81, 26, v34
	v_or_b32_e32 v82, 27, v35
	v_min3_u32 v80, v80, v81, v82
	v_or_b32_e32 v81, 28, v36
	v_or_b32_e32 v82, 29, v37
	v_min3_u32 v80, v80, v81, v82
	v_or_b32_e32 v81, 30, v38
	v_or_b32_e32 v82, 31, v39
	v_min3_u32 v80, v80, v81, v82
	v_mul_f64 v[86:87], v[86:87], v[84:85]
	v_mul_f32_e32 v24, s14, v24
	v_mul_f32_e32 v25, s14, v25
	v_mul_f32_e32 v26, s14, v26
	v_mul_f32_e32 v27, s14, v27
	v_mul_f32_e32 v28, s14, v28
	v_mul_f32_e32 v29, s14, v29
	v_mul_f32_e32 v30, s14, v30
	v_mul_f32_e32 v31, s14, v31
	v_mul_f32_e32 v32, s14, v32
	v_mul_f32_e32 v33, s14, v33
	v_mul_f32_e32 v34, s14, v34
	v_mul_f32_e32 v35, s14, v35
	v_mul_f32_e32 v36, s14, v36
	v_mul_f32_e32 v37, s14, v37
	v_mul_f32_e32 v38, s14, v38
	v_mul_f32_e32 v39, s14, v39
	v_exp_f32_e32 v24, v24
	v_exp_f32_e32 v25, v25
	v_exp_f32_e32 v26, v26
	v_exp_f32_e32 v27, v27
	v_exp_f32_e32 v28, v28
	v_exp_f32_e32 v29, v29
	v_exp_f32_e32 v30, v30
	v_exp_f32_e32 v31, v31
	v_exp_f32_e32 v32, v32
	v_exp_f32_e32 v33, v33
	v_exp_f32_e32 v34, v34
	v_exp_f32_e32 v35, v35
	v_exp_f32_e32 v36, v36
	v_exp_f32_e32 v37, v37
	v_exp_f32_e32 v38, v38
	v_exp_f32_e32 v39, v39
	v_add_f32_e32 v78, v24, v26
	v_add_f32_e32 v79, v25, v27
	v_add_f32_e32 v78, v78, v28
	v_add_f32_e32 v79, v79, v29
	v_add_f32_e32 v78, v78, v30
	v_add_f32_e32 v79, v79, v31
	v_add_f32_e32 v78, v78, v32
	v_add_f32_e32 v79, v79, v33
	v_add_f32_e32 v78, v78, v34
	v_add_f32_e32 v79, v79, v35
	v_add_f32_e32 v78, v78, v36
	v_add_f32_e32 v79, v79, v37
	v_add_f32_e32 v78, v78, v38
	v_add_f32_e32 v79, v79, v39
	v_add_f32_e32 v78, v78, v79
	v_cvt_f64_f32_e32 v[84:85], v78
	v_cndmask_b32_e64 v75, v75, v80, s[20:21]
	v_mov_b32_e32 v73, v77
	v_add_f64 v[86:87], v[86:87], v[84:85]
	s_waitcnt vmcnt(17)
	v_max3_f32 v76, v40, v41, v42
	v_max3_f32 v76, v76, v43, v44
	v_max3_f32 v76, v76, v45, v46
	v_max3_f32 v76, v76, v47, v48
	v_max3_f32 v76, v76, v49, v50
	v_max3_f32 v76, v76, v51, v52
	v_max3_f32 v76, v76, v53, v54
	v_max_f32_e32 v76, v76, v55
	v_max_f32_e32 v77, v73, v76
	v_cmp_gt_f32_e64 s[20:21], v76, v73
	v_sub_f32_e32 v83, v73, v77
	v_mul_f32_e32 v83, s14, v83
	v_exp_f32_e32 v83, v83
	v_sub_f32_e32 v40, v40, v77
	v_sub_f32_e32 v41, v41, v77
	v_sub_f32_e32 v42, v42, v77
	v_sub_f32_e32 v43, v43, v77
	v_sub_f32_e32 v44, v44, v77
	v_sub_f32_e32 v45, v45, v77
	v_sub_f32_e32 v46, v46, v77
	v_sub_f32_e32 v47, v47, v77
	v_sub_f32_e32 v48, v48, v77
	v_sub_f32_e32 v49, v49, v77
	v_sub_f32_e32 v50, v50, v77
	v_sub_f32_e32 v51, v51, v77
	v_sub_f32_e32 v52, v52, v77
	v_sub_f32_e32 v53, v53, v77
	v_sub_f32_e32 v54, v54, v77
	v_sub_f32_e32 v55, v55, v77
	v_cvt_f64_f32_e32 v[84:85], v83
	v_or_b32_e32 v81, 32, v40
	v_or_b32_e32 v82, 33, v41
	v_min_u32_e32 v80, v81, v82
	v_or_b32_e32 v81, 34, v42
	v_or_b32_e32 v82, 35, v43
	v_min3_u32 v80, v80, v81, v82
	v_or_b32_e32 v81, 36, v44
	v_or_b32_e32 v82, 37, v45
	v_min3_u32 v80, v80, v81, v82
	v_or_b32_e32 v81, 38, v46
	v_or_b32_e32 v82, 39, v47
	v_min3_u32 v80, v80, v81, v82
	v_or_b32_e32 v81, 40, v48
	v_or_b32_e32 v82, 41, v49
	v_min3_u32 v80, v80, v81, v82
	v_or_b32_e32 v81, 42, v50
	v_or_b32_e32 v82, 43, v51
	v_min3_u32 v80, v80, v81, v82
	v_or_b32_e32 v81, 44, v52
	v_or_b32_e32 v82, 45, v53
	v_min3_u32 v80, v80, v81, v82
	v_or_b32_e32 v81, 46, v54
	v_or_b32_e32 v82, 47, v55
	v_min3_u32 v80, v80, v81, v82
	v_mul_f64 v[86:87], v[86:87], v[84:85]
	v_mul_f32_e32 v40, s14, v40
	v_mul_f32_e32 v41, s14, v41
	v_mul_f32_e32 v42, s14, v42
	v_mul_f32_e32 v43, s14, v43
	v_mul_f32_e32 v44, s14, v44
	v_mul_f32_e32 v45, s14, v45
	v_mul_f32_e32 v46, s14, v46
	v_mul_f32_e32 v47, s14, v47
	v_mul_f32_e32 v48, s14, v48
	v_mul_f32_e32 v49, s14, v49
	v_mul_f32_e32 v50, s14, v50
	v_mul_f32_e32 v51, s14, v51
	v_mul_f32_e32 v52, s14, v52
	v_mul_f32_e32 v53, s14, v53
	v_mul_f32_e32 v54, s14, v54
	v_mul_f32_e32 v55, s14, v55
	v_exp_f32_e32 v40, v40
	v_exp_f32_e32 v41, v41
	v_exp_f32_e32 v42, v42
	v_exp_f32_e32 v43, v43
	v_exp_f32_e32 v44, v44
	v_exp_f32_e32 v45, v45
	v_exp_f32_e32 v46, v46
	v_exp_f32_e32 v47, v47
	v_exp_f32_e32 v48, v48
	v_exp_f32_e32 v49, v49
	v_exp_f32_e32 v50, v50
	v_exp_f32_e32 v51, v51
	v_exp_f32_e32 v52, v52
	v_exp_f32_e32 v53, v53
	v_exp_f32_e32 v54, v54
	v_exp_f32_e32 v55, v55
	v_add_f32_e32 v78, v40, v42
	v_add_f32_e32 v79, v41, v43
	v_add_f32_e32 v78, v78, v44
	v_add_f32_e32 v79, v79, v45
	v_add_f32_e32 v78, v78, v46
	v_add_f32_e32 v79, v79, v47
	v_add_f32_e32 v78, v78, v48
	v_add_f32_e32 v79, v79, v49
	v_add_f32_e32 v78, v78, v50
	v_add_f32_e32 v79, v79, v51
	v_add_f32_e32 v78, v78, v52
	v_add_f32_e32 v79, v79, v53
	v_add_f32_e32 v78, v78, v54
	v_add_f32_e32 v79, v79, v55
	v_add_f32_e32 v78, v78, v79
	v_cvt_f64_f32_e32 v[84:85], v78
	v_cndmask_b32_e64 v75, v75, v80, s[20:21]
	v_mov_b32_e32 v73, v77
	v_add_f64 v[86:87], v[86:87], v[84:85]
	s_waitcnt vmcnt(3)
	v_max3_f32 v76, v56, v57, v58
	v_max3_f32 v76, v76, v59, v60
	v_max3_f32 v76, v76, v61, v62
	v_max3_f32 v76, v76, v63, v64
	v_max3_f32 v76, v76, v65, v66
	v_max3_f32 v76, v76, v67, v68
	v_max_f32_e32 v76, v76, v69
	v_max_f32_e32 v77, v73, v76
	v_cmp_gt_f32_e64 s[20:21], v76, v73
	v_sub_f32_e32 v83, v73, v77
	v_mul_f32_e32 v83, s14, v83
	v_exp_f32_e32 v83, v83
	v_sub_f32_e32 v56, v56, v77
	v_sub_f32_e32 v57, v57, v77
	v_sub_f32_e32 v58, v58, v77
	v_sub_f32_e32 v59, v59, v77
	v_sub_f32_e32 v60, v60, v77
	v_sub_f32_e32 v61, v61, v77
	v_sub_f32_e32 v62, v62, v77
	v_sub_f32_e32 v63, v63, v77
	v_sub_f32_e32 v64, v64, v77
	v_sub_f32_e32 v65, v65, v77
	v_sub_f32_e32 v66, v66, v77
	v_sub_f32_e32 v67, v67, v77
	v_sub_f32_e32 v68, v68, v77
	v_sub_f32_e32 v69, v69, v77
	v_cvt_f64_f32_e32 v[84:85], v83
	v_or_b32_e32 v81, 48, v56
	v_or_b32_e32 v82, 49, v57
	v_min_u32_e32 v80, v81, v82
	v_or_b32_e32 v81, 50, v58
	v_or_b32_e32 v82, 51, v59
	v_min3_u32 v80, v80, v81, v82
	v_or_b32_e32 v81, 52, v60
	v_or_b32_e32 v82, 53, v61
	v_min3_u32 v80, v80, v81, v82
	v_or_b32_e32 v81, 54, v62
	v_or_b32_e32 v82, 55, v63
	v_min3_u32 v80, v80, v81, v82
	v_or_b32_e32 v81, 56, v64
	v_or_b32_e32 v82, 57, v65
	v_min3_u32 v80, v80, v81, v82
	v_or_b32_e32 v81, 58, v66
	v_or_b32_e32 v82, 59, v67
	v_min3_u32 v80, v80, v81, v82
	v_or_b32_e32 v81, 60, v68
	v_or_b32_e32 v82, 61, v69
	v_min3_u32 v80, v80, v81, v82
	v_mul_f64 v[86:87], v[86:87], v[84:85]
	v_mul_f32_e32 v56, s14, v56
	v_mul_f32_e32 v57, s14, v57
	v_mul_f32_e32 v58, s14, v58
	v_mul_f32_e32 v59, s14, v59
	v_mul_f32_e32 v60, s14, v60
	v_mul_f32_e32 v61, s14, v61
	v_mul_f32_e32 v62, s14, v62
	v_mul_f32_e32 v63, s14, v63
	v_mul_f32_e32 v64, s14, v64
	v_mul_f32_e32 v65, s14, v65
	v_mul_f32_e32 v66, s14, v66
	v_mul_f32_e32 v67, s14, v67
	v_mul_f32_e32 v68, s14, v68
	v_mul_f32_e32 v69, s14, v69
	v_exp_f32_e32 v56, v56
	v_exp_f32_e32 v57, v57
	v_exp_f32_e32 v58, v58
	v_exp_f32_e32 v59, v59
	v_exp_f32_e32 v60, v60
	v_exp_f32_e32 v61, v61
	v_exp_f32_e32 v62, v62
	v_exp_f32_e32 v63, v63
	v_exp_f32_e32 v64, v64
	v_exp_f32_e32 v65, v65
	v_exp_f32_e32 v66, v66
	v_exp_f32_e32 v67, v67
	v_exp_f32_e32 v68, v68
	v_exp_f32_e32 v69, v69
	v_add_f32_e32 v78, v56, v58
	v_add_f32_e32 v79, v57, v59
	v_add_f32_e32 v78, v78, v60
	v_add_f32_e32 v79, v79, v61
	v_add_f32_e32 v78, v78, v62
	v_add_f32_e32 v79, v79, v63
	v_add_f32_e32 v78, v78, v64
	v_add_f32_e32 v79, v79, v65
	v_add_f32_e32 v78, v78, v66
	v_add_f32_e32 v79, v79, v67
	v_add_f32_e32 v78, v78, v68
	v_add_f32_e32 v79, v79, v69
	v_add_f32_e32 v78, v78, v79
	v_cvt_f64_f32_e32 v[84:85], v78
	v_cndmask_b32_e64 v75, v75, v80, s[20:21]
	v_mov_b32_e32 v73, v77
	v_add_f64 v[86:87], v[86:87], v[84:85]
	s_waitcnt vmcnt(0)
	v_max3_f32 v76, v70, v71, v72
	v_max_f32_e32 v77, v73, v76
	v_cmp_gt_f32_e64 s[20:21], v76, v73
	v_sub_f32_e32 v83, v73, v77
	v_mul_f32_e32 v83, s14, v83
	v_exp_f32_e32 v83, v83
	v_sub_f32_e32 v70, v70, v77
	v_sub_f32_e32 v71, v71, v77
	v_sub_f32_e32 v72, v72, v77
	v_cvt_f64_f32_e32 v[84:85], v83
	v_or_b32_e32 v81, 62, v70
	v_or_b32_e32 v82, 63, v71
	v_min_u32_e32 v80, v81, v82
	v_or_b32_e32 v81, 64, v72
	v_min_u32_e32 v80, v80, v81
	v_mul_f64 v[86:87], v[86:87], v[84:85]
	v_mul_f32_e32 v70, s14, v70
	v_mul_f32_e32 v71, s14, v71
	v_mul_f32_e32 v72, s14, v72
	v_exp_f32_e32 v70, v70
	v_exp_f32_e32 v71, v71
	v_exp_f32_e32 v72, v72
	v_add_f32_e32 v78, v70, v71
	v_add_f32_e32 v78, v78, v72
	v_cvt_f64_f32_e32 v[84:85], v78
	v_cndmask_b32_e64 v75, v75, v80, s[20:21]
	v_mov_b32_e32 v73, v77
	v_add_f64 v[86:87], v[86:87], v[84:85]
	v_rcp_f64_e32 v[88:89], v[86:87]
	v_cmp_gt_u32_e32 vcc, 64, v75
	s_and_b64 vcc, vcc, s[36:37]
	v_fma_f64 v[90:91], -v[86:87], v[88:89], 1.0
	v_fma_f64 v[88:89], v[90:91], v[88:89], v[88:89]
	v_cvt_f32_f64_e32 v3, v[88:89]
	v_cndmask_b32_e32 v74, 0, v3, vcc
	global_store_dwordx2 v98, v[74:75], s[6:7]

.LBB1_49:
	s_or_b64 exec, exec, s[0:1]
	s_lshl_b32 s0, s33, 2
	s_add_u32 s0, s38, s0
	s_addc_u32 s1, s39, 0
	s_mov_b32 s2, 0x138800
	s_mov_b32 s18, 0
	v_lshlrev_b32_e32 v1, 1, v0
	v_xor_b32_e32 v8, 0x7fe, v1
	v_lshlrev_b32_e32 v9, 2, v8
	v_mov_b32_e32 v5, v4
	v_cmp_gt_u32_e32 vcc, 8, v0
	v_lshlrev_b32_e32 v27, 2, v0
	ds_write_b64 v9, v[4:5]
	s_and_saveexec_b64 s[0:1], vcc
	v_mov_b32_e32 v1, 0
	ds_write_b32 v27, v1 offset:8192
	s_or_b64 exec, exec, s[0:1]
	v_cmp_gt_u32_e64 s[0:1], 17, v0
	s_and_saveexec_b64 s[2:3], s[0:1]
	v_mov_b32_e32 v1, 0
	ds_write_b32 v27, v1 offset:48288
	s_or_b64 exec, exec, s[2:3]
	v_lshrrev_b32_e32 v34, 6, v0
	v_and_b32_e32 v1, 63, v0
	s_waitcnt lgkmcnt(0)
	s_barrier
	v_cmp_gt_u32_e32 vcc, 17, v1
	v_cmp_gt_u32_e64 s[2:3], v1, v34
	s_and_b64 s[16:17], vcc, s[2:3]
	s_waitcnt vmcnt(3)
	v_cmp_eq_u32_e32 vcc, 0, v2
	s_waitcnt vmcnt(2)
	v_cmp_eq_u32_e64 s[2:3], 0, v24
	s_waitcnt vmcnt(1)
	v_cmp_eq_u32_e64 s[4:5], 0, v22
	s_waitcnt vmcnt(0)
	v_cmp_eq_u32_e64 s[6:7], 0, v20
	v_cmp_eq_u32_e64 s[8:9], 0, v18
	v_mov_b32_e32 v4, 0
	v_lshlrev_b32_e32 v30, 2, v34
	v_lshlrev_b32_e32 v15, 2, v1
	s_xor_b64 s[14:15], vcc, -1
	v_mov_b32_e32 v16, 1
	s_xor_b64 s[12:13], s[2:3], -1
	s_xor_b64 s[10:11], s[4:5], -1
	s_xor_b64 s[6:7], s[6:7], -1
	s_xor_b64 s[4:5], s[8:9], -1
	s_movk_i32 s22, 0x12c
	v_mov_b32_e32 v5, v4
	s_branch .LBB1_56

.LBB1_74:
	s_or_b64 exec, exec, s[0:1]
	v_mov_b32_e32 v4, 0
	s_waitcnt lgkmcnt(0)
	s_barrier
	ds_read_b64 v[4:5], v4 offset:48432
	v_lshlrev_b32_e32 v6, 7, v0
	s_mov_b64 s[0:1], exec
	s_waitcnt lgkmcnt(0)
	v_cmp_ge_u32_e32 vcc, v14, v4
	s_and_b64 s[14:15], s[14:15], vcc
	v_cmp_ge_u32_e32 vcc, v13, v4
	s_and_b64 s[12:13], s[12:13], vcc
	v_cmp_ge_u32_e32 vcc, v12, v4
	s_and_b64 s[10:11], s[10:11], vcc
	v_cmp_ge_u32_e32 vcc, v11, v4
	s_and_b64 s[6:7], s[6:7], vcc
	v_cmp_ge_u32_e32 vcc, v10, v4
	s_and_b64 s[4:5], s[4:5], vcc
	v_mov_b32_e32 v7, 1
	v_lshlrev_b32_e32 v14, 2, v14
	v_lshlrev_b32_e32 v13, 2, v13
	v_lshlrev_b32_e32 v12, 2, v12
	v_lshlrev_b32_e32 v11, 2, v11
	v_lshlrev_b32_e32 v10, 2, v10
	s_mov_b64 exec, s[14:15]
	ds_add_rtn_u32 v58, v14, v7
	s_mov_b64 exec, s[12:13]
	ds_add_rtn_u32 v59, v13, v7
	s_mov_b64 exec, s[10:11]
	ds_add_rtn_u32 v60, v12, v7
	s_mov_b64 exec, s[6:7]
	ds_add_rtn_u32 v61, v11, v7
	s_mov_b64 exec, s[4:5]
	ds_add_rtn_u32 v62, v10, v7
	s_mov_b64 exec, s[0:1]
	s_waitcnt lgkmcnt(0)
	v_sub_u32_e32 v8, 0xfff80, v6
	v_or_b32_e32 v8, v3, v8
	v_mov_b32_e32 v9, v2
	v_lshlrev_b32_e32 v58, 3, v58
	s_mov_b64 exec, s[14:15]
	ds_write_b64 v58, v[8:9] offset:8224
	s_mov_b64 exec, s[0:1]
	v_sub_u32_e32 v8, 0xdff80, v6
	v_or_b32_e32 v8, v25, v8
	v_mov_b32_e32 v9, v24
	v_lshlrev_b32_e32 v59, 3, v59
	s_mov_b64 exec, s[12:13]
	ds_write_b64 v59, v[8:9] offset:8224
	s_mov_b64 exec, s[0:1]
	v_sub_u32_e32 v8, 0xbff80, v6
	v_or_b32_e32 v8, v23, v8
	v_mov_b32_e32 v9, v22
	v_lshlrev_b32_e32 v60, 3, v60
	s_mov_b64 exec, s[10:11]
	ds_write_b64 v60, v[8:9] offset:8224
	s_mov_b64 exec, s[0:1]
	v_sub_u32_e32 v8, 0x9ff80, v6
	v_or_b32_e32 v8, v21, v8
	v_mov_b32_e32 v9, v20
	v_lshlrev_b32_e32 v61, 3, v61
	s_mov_b64 exec, s[6:7]
	ds_write_b64 v61, v[8:9] offset:8224
	s_mov_b64 exec, s[0:1]
	v_sub_u32_e32 v8, 0x7ff80, v6
	v_or_b32_e32 v8, v19, v8
	v_mov_b32_e32 v9, v18
	v_lshlrev_b32_e32 v62, 3, v62
	s_mov_b64 exec, s[4:5]
	ds_write_b64 v62, v[8:9] offset:8224
	s_mov_b64 exec, s[0:1]
	v_cmp_lt_i32_e32 vcc, v0, v5
	s_waitcnt lgkmcnt(0)
	s_barrier
	s_and_saveexec_b64 s[0:1], vcc
	s_cbranch_execz .LBB1_93
	s_mov_b64 s[2:3], 0
	s_movk_i32 s8, 0x12c
	s_mov_b32 s9, 0x51eb851f
	s_movk_i32 s10, 0xff9c
	s_mov_b32 s11, 0x43480000
	s_mov_b32 s12, 0x43c80000
	s_mov_b32 s13, 0x3ba3d70a
	s_mov_b32 s14, 0x3b23d70a
	v_mov_b32_e32 v4, 1.0
	v_mov_b32_e32 v10, 0x2020
	v_mov_b32_e32 v11, v0
	s_branch .LBB1_87

.LBB1_91:
	s_or_b64 exec, exec, s[4:5]
	v_cmp_gt_i32_e32 vcc, s8, v9
	s_and_saveexec_b64 s[4:5], vcc
	s_cbranch_execz .LBB1_86
	v_lshrrev_b32_e32 v8, 7, v6
	v_sub_u32_e32 v8, 0x1fff, v8
	v_mul_hi_i32 v12, v8, s9
	v_and_b32_e32 v6, 0x7f, v6
	v_lshrrev_b32_e32 v13, 31, v12
	v_ashrrev_i32_e32 v12, 5, v12
	v_min_u32_e32 v6, 63, v6
	v_add_u32_e32 v12, v12, v13
	v_mad_i32_i24 v8, v12, s10, v8
	v_lshrrev_b32_e32 v13, 3, v6
	v_and_b32_e32 v6, 7, v6
	v_lshl_or_b32 v6, v8, 3, v6
	v_lshl_or_b32 v8, v12, 3, v13
	v_add_u32_e32 v8, 0xffffff38, v8
	v_cvt_f32_i32_e32 v8, v8
	v_lshl_add_u32 v12, v9, 1, v9
	v_ashrrev_i32_e32 v13, 31, v12
	v_cvt_f32_i32_e32 v6, v6
	v_lshl_add_u64 v[16:17], v[12:13], 2, s[38:39]
	v_add_f32_e32 v6, 0xc3c80000, v6
	v_mul_f32_e32 v13, s13, v8
	v_mul_f32_e32 v12, s14, v6
	v_fma_f32 v15, -v13, s11, v8
	v_fma_f32 v26, -v12, s12, v6
	v_fma_f32 v13, v15, s13, v13
	v_fma_f32 v12, v26, s14, v12
	v_mov_b32_e32 v14, v7
	v_ashrrev_i32_e32 v7, 31, v9
	v_mov_b32_e32 v6, v9
	v_lshl_add_u64 v[6:7], v[6:7], 2, s[36:37]
	global_store_dwordx3 v[16:17], v[12:14], off
	global_store_dword v[6:7], v4, off
	s_branch .LBB1_86

	.amdhsa_kernel _Z13select_kernelPK15HIP_vector_typeIjLj2EEPKfPf
		.amdhsa_group_segment_fixed_size 49664
		.amdhsa_private_segment_fixed_size 0
		.amdhsa_kernarg_size 24
		.amdhsa_user_sgpr_count 2
		.amdhsa_user_sgpr_dispatch_ptr 0
		.amdhsa_user_sgpr_queue_ptr 0
		.amdhsa_user_sgpr_kernarg_segment_ptr 1
		.amdhsa_user_sgpr_dispatch_id 0
		.amdhsa_user_sgpr_kernarg_preload_length 0
		.amdhsa_user_sgpr_kernarg_preload_offset 0
		.amdhsa_user_sgpr_private_segment_size 0
		.amdhsa_uses_dynamic_stack 0
		.amdhsa_enable_private_segment 0
		.amdhsa_system_sgpr_workgroup_id_x 1
		.amdhsa_system_sgpr_workgroup_id_y 0
		.amdhsa_system_sgpr_workgroup_id_z 0
		.amdhsa_system_sgpr_workgroup_info 0
		.amdhsa_system_vgpr_workitem_id 0
		.amdhsa_next_free_vgpr 63
		.amdhsa_next_free_sgpr 52
		.amdhsa_accum_offset 64
		.amdhsa_reserve_vcc 1
		.amdhsa_float_round_mode_32 0
		.amdhsa_float_round_mode_16_64 0
		.amdhsa_float_denorm_mode_32 3
		.amdhsa_float_denorm_mode_16_64 3
		.amdhsa_dx10_clamp 1
		.amdhsa_ieee_mode 1
		.amdhsa_fp16_overflow 0
		.amdhsa_tg_split 0
		.amdhsa_exception_fp_ieee_invalid_op 0
		.amdhsa_exception_fp_denorm_src 0
		.amdhsa_exception_fp_ieee_div_zero 0
		.amdhsa_exception_fp_ieee_overflow 0
		.amdhsa_exception_fp_ieee_underflow 0
		.amdhsa_exception_fp_ieee_inexact 0
		.amdhsa_exception_int_div_zero 0
	.end_amdhsa_kernel

amdhsa.kernels:
  - .agpr_count:     0
    .args:
      - .actual_access:  read_only
        .address_space:  global
        .offset:         0
        .size:           8
        .value_kind:     global_buffer
      - .actual_access:  write_only
        .address_space:  global
        .offset:         8
        .size:           8
        .value_kind:     global_buffer
      - .actual_access:  read_only
        .address_space:  global
        .offset:         16
        .size:           8
        .value_kind:     global_buffer
      - .actual_access:  read_only
        .address_space:  global
        .offset:         24
        .size:           8
        .value_kind:     global_buffer
    .group_segment_fixed_size: 0
    .kernarg_segment_align: 8
    .kernarg_segment_size: 32
    .language:       OpenCL C
    .language_version:
      - 2
      - 0
    .max_flat_workgroup_size: 640
    .name:           _Z12score_kernelPKfP15HIP_vector_typeIjLj2EES0_S0_
    .private_segment_fixed_size: 0
    .sgpr_count:     62
    .sgpr_spill_count: 0
    .symbol:         _Z12score_kernelPKfP15HIP_vector_typeIjLj2EES0_S0_.kd
    .uniform_work_group_size: 1
    .uses_dynamic_stack: false
    .vgpr_count:     100
    .vgpr_spill_count: 0
    .wavefront_size: 64
  - .agpr_count:     0
    .args:
      - .actual_access:  read_only
        .address_space:  global
        .offset:         0
        .size:           8
        .value_kind:     global_buffer
      - .actual_access:  read_only
        .address_space:  global
        .offset:         8
        .size:           8
        .value_kind:     global_buffer
      - .actual_access:  write_only
        .address_space:  global
        .offset:         16
        .size:           8
        .value_kind:     global_buffer
    .group_segment_fixed_size: 49664
    .kernarg_segment_align: 8
    .kernarg_segment_size: 24
    .language:       OpenCL C
    .language_version:
      - 2
      - 0
    .max_flat_workgroup_size: 1024
    .name:           _Z13select_kernelPK15HIP_vector_typeIjLj2EEPKfPf
    .private_segment_fixed_size: 0
    .sgpr_count:     58
    .sgpr_spill_count: 0
    .symbol:         _Z13select_kernelPK15HIP_vector_typeIjLj2EEPKfPf.kd
    .uniform_work_group_size: 1
    .uses_dynamic_stack: false
    .vgpr_count:     63
    .vgpr_spill_count: 0
    .wavefront_size: 64
